# BEST + one static priority raise for waves 0-3 instead of per-segment s_setprio toggles in all five K-loops
# baseline (speedup 1.0000x reference)
; #define LAS __attribute__((address_space(3)))
; __global__ void __launch_bounds__(NTHREADS, 2) hymba_fwd(Params P) {
;     extern __shared__ __attribute__((aligned(16))) unsigned char lds_raw[];
;     LAS unsigned char* lds = (LAS unsigned char*)lds_raw;
;     const int tid = threadIdx.x, blk = blockIdx.x, G = gridDim.x;
_Z9hymba_fwd6Params:
	v_readfirstlane_b32 s3, v0
	s_nop 3
	s_cmpk_lt_u32 s3, 0x100
	s_cbranch_scc0 .Lprio_lo
	s_setprio 1
